# conformer conv: the 29 serialised LDS tap reads (read, lgkmcnt(0), shift, FMAs) kept 8 deep in free registers with counted waits
# speedup vs baseline: 1.0103x; 1.0042x over previous
.LBB0_2165:
	ds_read_u16 v29, v22
	ds_read_u16 v30, v22 offset:1024
	ds_read_u16 v31, v22 offset:2048
	ds_read_u16 v32, v22 offset:3072
	ds_read_u16 v33, v22 offset:4096
	ds_read_u16 v34, v22 offset:5120
	ds_read_u16 v35, v22 offset:6144
	ds_read_u16 v36, v22 offset:7168
	s_waitcnt lgkmcnt(7)
	v_lshlrev_b32_e32 v29, 16, v29
	v_fma_f32 v29, v51, v29, v52
	s_waitcnt lgkmcnt(6)
	v_lshlrev_b32_e32 v30, 16, v30
	v_fmac_f32_e32 v29, v54, v30
	v_fma_f32 v30, v51, v30, v52
	s_waitcnt lgkmcnt(5)
	v_lshlrev_b32_e32 v31, 16, v31
	v_fmac_f32_e32 v29, v55, v31
	v_fmac_f32_e32 v30, v54, v31
	v_fma_f32 v31, v51, v31, v52
	s_waitcnt lgkmcnt(4)
	v_lshlrev_b32_e32 v32, 16, v32
	ds_read_u16 v37, v22 offset:8192
	ds_read_u16 v38, v22 offset:9216
	ds_read_u16 v39, v22 offset:10240
	ds_read_u16 v40, v22 offset:11264
	ds_read_u16 v41, v22 offset:12288
	ds_read_u16 v42, v22 offset:13312
	ds_read_u16 v43, v22 offset:14336
	ds_read_u16 v44, v22 offset:15360
	v_fmac_f32_e32 v29, v56, v32
	v_fmac_f32_e32 v30, v55, v32
	v_fmac_f32_e32 v31, v54, v32
	v_fma_f32 v32, v51, v32, v52
	s_waitcnt lgkmcnt(11)
	v_lshlrev_b32_e32 v33, 16, v33
	v_fmac_f32_e32 v29, v57, v33
	v_fmac_f32_e32 v30, v56, v33
	v_fmac_f32_e32 v31, v55, v33
	v_fmac_f32_e32 v32, v54, v33
	v_fma_f32 v33, v51, v33, v52
	s_waitcnt lgkmcnt(10)
	v_lshlrev_b32_e32 v34, 16, v34
	v_fmac_f32_e32 v29, v58, v34
	v_fmac_f32_e32 v30, v57, v34
	v_fmac_f32_e32 v31, v56, v34
	v_fmac_f32_e32 v32, v55, v34
	v_fmac_f32_e32 v33, v54, v34
	v_fma_f32 v34, v51, v34, v52
	s_waitcnt lgkmcnt(9)
	v_lshlrev_b32_e32 v35, 16, v35
	v_fmac_f32_e32 v29, v59, v35
	v_fmac_f32_e32 v30, v58, v35
	v_fmac_f32_e32 v31, v57, v35
	v_fmac_f32_e32 v32, v56, v35
	v_fmac_f32_e32 v33, v55, v35
	v_fmac_f32_e32 v34, v54, v35
	v_fma_f32 v35, v51, v35, v52
	s_waitcnt lgkmcnt(8)
	v_lshlrev_b32_e32 v36, 16, v36
	v_fmac_f32_e32 v29, v60, v36
	v_fmac_f32_e32 v30, v59, v36
	v_fmac_f32_e32 v31, v58, v36
	v_fmac_f32_e32 v32, v57, v36
	v_fmac_f32_e32 v33, v56, v36
	v_fmac_f32_e32 v34, v55, v36
	v_fmac_f32_e32 v35, v54, v36
	v_fma_f32 v36, v51, v36, v52
	s_waitcnt lgkmcnt(7)
	v_lshlrev_b32_e32 v37, 16, v37
	v_fmac_f32_e32 v29, v61, v37
	v_fmac_f32_e32 v30, v60, v37
	v_fmac_f32_e32 v31, v59, v37
	v_fmac_f32_e32 v32, v58, v37
	v_fmac_f32_e32 v33, v57, v37
	v_fmac_f32_e32 v34, v56, v37
	v_fmac_f32_e32 v35, v55, v37
	v_fmac_f32_e32 v36, v54, v37
	v_fma_f32 v37, v51, v37, v52
	s_waitcnt lgkmcnt(6)
	v_lshlrev_b32_e32 v38, 16, v38
	v_fmac_f32_e32 v29, v62, v38
	v_fmac_f32_e32 v30, v61, v38
	v_fmac_f32_e32 v31, v60, v38
	v_fmac_f32_e32 v32, v59, v38
	v_fmac_f32_e32 v33, v58, v38
	v_fmac_f32_e32 v34, v57, v38
	v_fmac_f32_e32 v35, v56, v38
	v_fmac_f32_e32 v36, v55, v38
	v_fmac_f32_e32 v37, v54, v38
	v_fma_f32 v38, v51, v38, v52
	s_waitcnt lgkmcnt(5)
	v_lshlrev_b32_e32 v39, 16, v39
	v_fmac_f32_e32 v29, v63, v39
	v_fmac_f32_e32 v30, v62, v39
	v_fmac_f32_e32 v31, v61, v39
	v_fmac_f32_e32 v32, v60, v39
	v_fmac_f32_e32 v33, v59, v39
	v_fmac_f32_e32 v34, v58, v39
	v_fmac_f32_e32 v35, v57, v39
	v_fmac_f32_e32 v36, v56, v39
	v_fmac_f32_e32 v37, v55, v39
	v_fmac_f32_e32 v38, v54, v39
	v_fma_f32 v39, v51, v39, v52
	s_waitcnt lgkmcnt(4)
	v_lshlrev_b32_e32 v40, 16, v40
	ds_read_u16 v45, v22 offset:16384
	v_fmac_f32_e32 v29, v64, v40
	v_fmac_f32_e32 v30, v63, v40
	v_fmac_f32_e32 v31, v62, v40
	v_fmac_f32_e32 v32, v61, v40
	v_fmac_f32_e32 v33, v60, v40
	v_fmac_f32_e32 v34, v59, v40
	v_fmac_f32_e32 v35, v58, v40
	v_fmac_f32_e32 v36, v57, v40
	v_fmac_f32_e32 v37, v56, v40
	v_fmac_f32_e32 v38, v55, v40
	v_fmac_f32_e32 v39, v54, v40
	v_fma_f32 v40, v51, v40, v52
	s_waitcnt lgkmcnt(4)
	v_lshlrev_b32_e32 v41, 16, v41
	v_fmac_f32_e32 v29, v65, v41
	v_fmac_f32_e32 v30, v64, v41
	v_fmac_f32_e32 v31, v63, v41
	v_fmac_f32_e32 v32, v62, v41
	v_fmac_f32_e32 v33, v61, v41
	v_fmac_f32_e32 v34, v60, v41
	v_fmac_f32_e32 v35, v59, v41
	v_fmac_f32_e32 v36, v58, v41
	v_fmac_f32_e32 v37, v57, v41
	v_fmac_f32_e32 v38, v56, v41
	v_fmac_f32_e32 v39, v55, v41
	v_fmac_f32_e32 v40, v54, v41
	v_fma_f32 v41, v51, v41, v52
	s_waitcnt lgkmcnt(3)
	v_lshlrev_b32_e32 v42, 16, v42
	v_fmac_f32_e32 v29, v66, v42
	v_fmac_f32_e32 v30, v65, v42
	v_fmac_f32_e32 v31, v64, v42
	v_fmac_f32_e32 v32, v63, v42
	v_fmac_f32_e32 v33, v62, v42
	v_fmac_f32_e32 v34, v61, v42
	v_fmac_f32_e32 v35, v60, v42
	v_fmac_f32_e32 v36, v59, v42
	v_fmac_f32_e32 v37, v58, v42
	v_fmac_f32_e32 v38, v57, v42
	v_fmac_f32_e32 v39, v56, v42
	v_fmac_f32_e32 v40, v55, v42
	v_fmac_f32_e32 v41, v54, v42
	v_fma_f32 v42, v51, v42, v52
	s_waitcnt lgkmcnt(2)
	v_lshlrev_b32_e32 v43, 16, v43
	v_fmac_f32_e32 v29, v67, v43
	v_fmac_f32_e32 v30, v66, v43
	v_fmac_f32_e32 v31, v65, v43
	v_fmac_f32_e32 v32, v64, v43
	v_fmac_f32_e32 v33, v63, v43
	v_fmac_f32_e32 v34, v62, v43
	v_fmac_f32_e32 v35, v61, v43
	v_fmac_f32_e32 v36, v60, v43
	v_fmac_f32_e32 v37, v59, v43
	v_fmac_f32_e32 v38, v58, v43
	v_fmac_f32_e32 v39, v57, v43
	v_fmac_f32_e32 v40, v56, v43
	v_fmac_f32_e32 v41, v55, v43
	v_fmac_f32_e32 v42, v54, v43
	v_fma_f32 v43, v51, v43, v52
	s_waitcnt lgkmcnt(1)
	v_lshlrev_b32_e32 v44, 16, v44
	v_fmac_f32_e32 v29, v68, v44
	v_fmac_f32_e32 v30, v67, v44
	v_fmac_f32_e32 v31, v66, v44
	v_fmac_f32_e32 v32, v65, v44
	v_fmac_f32_e32 v33, v64, v44
	v_fmac_f32_e32 v34, v63, v44
	v_fmac_f32_e32 v35, v62, v44
	v_fmac_f32_e32 v36, v61, v44
	v_fmac_f32_e32 v37, v60, v44
	v_fmac_f32_e32 v38, v59, v44
	v_fmac_f32_e32 v39, v58, v44
	v_fmac_f32_e32 v40, v57, v44
	v_fmac_f32_e32 v41, v56, v44
	v_fmac_f32_e32 v42, v55, v44
	v_fmac_f32_e32 v43, v54, v44
	v_fma_f32 v44, v51, v44, v52
	s_waitcnt lgkmcnt(0)
	v_lshlrev_b32_e32 v45, 16, v45
	v_fmac_f32_e32 v29, v69, v45
	v_fmac_f32_e32 v30, v68, v45
	v_fmac_f32_e32 v31, v67, v45
	v_fmac_f32_e32 v32, v66, v45
	v_fmac_f32_e32 v33, v65, v45
	v_fmac_f32_e32 v34, v64, v45
	v_fmac_f32_e32 v35, v63, v45
	v_fmac_f32_e32 v36, v62, v45
	v_fmac_f32_e32 v37, v61, v45
	v_fmac_f32_e32 v38, v60, v45
	v_fmac_f32_e32 v39, v59, v45
	v_fmac_f32_e32 v40, v58, v45
	v_fmac_f32_e32 v41, v57, v45
	v_fmac_f32_e32 v42, v56, v45
	v_fmac_f32_e32 v43, v55, v45
	v_fmac_f32_e32 v44, v54, v45
	ds_read_u16 v100, v22 offset:17408
	ds_read_u16 v101, v22 offset:18432
	ds_read_u16 v102, v22 offset:19456
	ds_read_u16 v103, v22 offset:20480
	ds_read_u16 v104, v22 offset:21504
	ds_read_u16 v105, v22 offset:22528
	ds_read_u16 v106, v22 offset:23552
	ds_read_u16 v107, v22 offset:24576
	s_waitcnt lgkmcnt(7)
	v_lshlrev_b32_e32 v45, 16, v100
	ds_read_u16 v100, v22 offset:25600
	v_fmac_f32_e32 v29, v70, v45
	v_fmac_f32_e32 v30, v69, v45
	v_fmac_f32_e32 v31, v68, v45
	v_fmac_f32_e32 v32, v67, v45
	v_fmac_f32_e32 v33, v66, v45
	v_fmac_f32_e32 v34, v65, v45
	v_fmac_f32_e32 v35, v64, v45
	v_fmac_f32_e32 v36, v63, v45
	v_fmac_f32_e32 v37, v62, v45
	v_fmac_f32_e32 v38, v61, v45
	v_fmac_f32_e32 v39, v60, v45
	v_fmac_f32_e32 v40, v59, v45
	v_fmac_f32_e32 v41, v58, v45
	v_fmac_f32_e32 v42, v57, v45
	v_fmac_f32_e32 v43, v56, v45
	v_fmac_f32_e32 v44, v55, v45
	s_waitcnt lgkmcnt(7)
	v_lshlrev_b32_e32 v45, 16, v101
	ds_read_u16 v101, v22 offset:26624
	v_fmac_f32_e32 v29, v71, v45
	v_fmac_f32_e32 v30, v70, v45
	v_fmac_f32_e32 v31, v69, v45
	v_fmac_f32_e32 v32, v68, v45
	v_fmac_f32_e32 v33, v67, v45
	v_fmac_f32_e32 v34, v66, v45
	v_fmac_f32_e32 v35, v65, v45
	v_fmac_f32_e32 v36, v64, v45
	v_fmac_f32_e32 v37, v63, v45
	v_fmac_f32_e32 v38, v62, v45
	v_fmac_f32_e32 v39, v61, v45
	v_fmac_f32_e32 v40, v60, v45
	v_fmac_f32_e32 v41, v59, v45
	v_fmac_f32_e32 v42, v58, v45
	v_fmac_f32_e32 v43, v57, v45
	v_fmac_f32_e32 v44, v56, v45
	s_waitcnt lgkmcnt(7)
	v_lshlrev_b32_e32 v45, 16, v102
	ds_read_u16 v102, v22 offset:27648
	v_fmac_f32_e32 v29, v72, v45
	v_fmac_f32_e32 v30, v71, v45
	v_fmac_f32_e32 v31, v70, v45
	v_fmac_f32_e32 v32, v69, v45
	v_fmac_f32_e32 v33, v68, v45
	v_fmac_f32_e32 v34, v67, v45
	v_fmac_f32_e32 v35, v66, v45
	v_fmac_f32_e32 v36, v65, v45
	v_fmac_f32_e32 v37, v64, v45
	v_fmac_f32_e32 v38, v63, v45
	v_fmac_f32_e32 v39, v62, v45
	v_fmac_f32_e32 v40, v61, v45
	v_fmac_f32_e32 v41, v60, v45
	v_fmac_f32_e32 v42, v59, v45
	v_fmac_f32_e32 v43, v58, v45
	v_fmac_f32_e32 v44, v57, v45
	s_waitcnt lgkmcnt(7)
	v_lshlrev_b32_e32 v45, 16, v103
	ds_read_u16 v103, v22 offset:28672
	v_fmac_f32_e32 v29, v73, v45
	v_fmac_f32_e32 v30, v72, v45
	v_fmac_f32_e32 v31, v71, v45
	v_fmac_f32_e32 v32, v70, v45
	v_fmac_f32_e32 v33, v69, v45
	v_fmac_f32_e32 v34, v68, v45
	v_fmac_f32_e32 v35, v67, v45
	v_fmac_f32_e32 v36, v66, v45
	v_fmac_f32_e32 v37, v65, v45
	v_fmac_f32_e32 v38, v64, v45
	v_fmac_f32_e32 v39, v63, v45
	v_fmac_f32_e32 v40, v62, v45
	v_fmac_f32_e32 v41, v61, v45
	v_fmac_f32_e32 v42, v60, v45
	v_fmac_f32_e32 v43, v59, v45
	v_fmac_f32_e32 v44, v58, v45
	s_waitcnt lgkmcnt(7)
	v_lshlrev_b32_e32 v45, 16, v104
	ds_read_u16 v104, v22 offset:29696
	v_fmac_f32_e32 v29, v74, v45
	v_fmac_f32_e32 v30, v73, v45
	v_fmac_f32_e32 v31, v72, v45
	v_fmac_f32_e32 v32, v71, v45
	v_fmac_f32_e32 v33, v70, v45
	v_fmac_f32_e32 v34, v69, v45
	v_fmac_f32_e32 v35, v68, v45
	v_fmac_f32_e32 v36, v67, v45
	v_fmac_f32_e32 v37, v66, v45
	v_fmac_f32_e32 v38, v65, v45
	v_fmac_f32_e32 v39, v64, v45
	v_fmac_f32_e32 v40, v63, v45
	v_fmac_f32_e32 v41, v62, v45
	v_fmac_f32_e32 v42, v61, v45
	v_fmac_f32_e32 v43, v60, v45
	v_fmac_f32_e32 v44, v59, v45
	s_waitcnt lgkmcnt(7)
	v_lshlrev_b32_e32 v45, 16, v105
	ds_read_u16 v105, v22 offset:30720
	v_fmac_f32_e32 v29, v75, v45
	v_fmac_f32_e32 v30, v74, v45
	v_fmac_f32_e32 v31, v73, v45
	v_fmac_f32_e32 v32, v72, v45
	v_fmac_f32_e32 v33, v71, v45
	v_fmac_f32_e32 v34, v70, v45
	v_fmac_f32_e32 v35, v69, v45
	v_fmac_f32_e32 v36, v68, v45
	v_fmac_f32_e32 v37, v67, v45
	v_fmac_f32_e32 v38, v66, v45
	v_fmac_f32_e32 v39, v65, v45
	v_fmac_f32_e32 v40, v64, v45
	v_fmac_f32_e32 v41, v63, v45
	v_fmac_f32_e32 v42, v62, v45
	v_fmac_f32_e32 v43, v61, v45
	v_fmac_f32_e32 v44, v60, v45
	s_waitcnt lgkmcnt(7)
	v_lshlrev_b32_e32 v45, 16, v106
	ds_read_u16 v106, v22 offset:31744
	v_fmac_f32_e32 v29, v76, v45
	v_fmac_f32_e32 v30, v75, v45
	v_fmac_f32_e32 v31, v74, v45
	v_fmac_f32_e32 v32, v73, v45
	v_fmac_f32_e32 v33, v72, v45
	v_fmac_f32_e32 v34, v71, v45
	v_fmac_f32_e32 v35, v70, v45
	v_fmac_f32_e32 v36, v69, v45
	v_fmac_f32_e32 v37, v68, v45
	v_fmac_f32_e32 v38, v67, v45
	v_fmac_f32_e32 v39, v66, v45
	v_fmac_f32_e32 v40, v65, v45
	v_fmac_f32_e32 v41, v64, v45
	v_fmac_f32_e32 v42, v63, v45
	v_fmac_f32_e32 v43, v62, v45
	v_fmac_f32_e32 v44, v61, v45
	s_waitcnt lgkmcnt(7)
	v_lshlrev_b32_e32 v45, 16, v107
	ds_read_u16 v107, v22 offset:32768
	v_fmac_f32_e32 v29, v77, v45
	v_fmac_f32_e32 v30, v76, v45
	v_fmac_f32_e32 v31, v75, v45
	v_fmac_f32_e32 v32, v74, v45
	v_fmac_f32_e32 v33, v73, v45
	v_fmac_f32_e32 v34, v72, v45
	v_fmac_f32_e32 v35, v71, v45
	v_fmac_f32_e32 v36, v70, v45
	v_fmac_f32_e32 v37, v69, v45
	v_fmac_f32_e32 v38, v68, v45
	v_fmac_f32_e32 v39, v67, v45
	v_fmac_f32_e32 v40, v66, v45
	v_fmac_f32_e32 v41, v65, v45
	v_fmac_f32_e32 v42, v64, v45
	v_fmac_f32_e32 v43, v63, v45
	v_fmac_f32_e32 v44, v62, v45
	s_waitcnt lgkmcnt(7)
	v_lshlrev_b32_e32 v45, 16, v100
	ds_read_u16 v100, v22 offset:33792
	v_fmac_f32_e32 v29, v78, v45
	v_fmac_f32_e32 v30, v77, v45
	v_fmac_f32_e32 v31, v76, v45
	v_fmac_f32_e32 v32, v75, v45
	v_fmac_f32_e32 v33, v74, v45
	v_fmac_f32_e32 v34, v73, v45
	v_fmac_f32_e32 v35, v72, v45
	v_fmac_f32_e32 v36, v71, v45
	v_fmac_f32_e32 v37, v70, v45
	v_fmac_f32_e32 v38, v69, v45
	v_fmac_f32_e32 v39, v68, v45
	v_fmac_f32_e32 v40, v67, v45
	v_fmac_f32_e32 v41, v66, v45
	v_fmac_f32_e32 v42, v65, v45
	v_fmac_f32_e32 v43, v64, v45
	v_fmac_f32_e32 v44, v63, v45
	s_waitcnt lgkmcnt(7)
	v_lshlrev_b32_e32 v45, 16, v101
	ds_read_u16 v101, v22 offset:34816
	v_fmac_f32_e32 v29, v79, v45
	v_fmac_f32_e32 v30, v78, v45
	v_fmac_f32_e32 v31, v77, v45
	v_fmac_f32_e32 v32, v76, v45
	v_fmac_f32_e32 v33, v75, v45
	v_fmac_f32_e32 v34, v74, v45
	v_fmac_f32_e32 v35, v73, v45
	v_fmac_f32_e32 v36, v72, v45
	v_fmac_f32_e32 v37, v71, v45
	v_fmac_f32_e32 v38, v70, v45
	v_fmac_f32_e32 v39, v69, v45
	v_fmac_f32_e32 v40, v68, v45
	v_fmac_f32_e32 v41, v67, v45
	v_fmac_f32_e32 v42, v66, v45
	v_fmac_f32_e32 v43, v65, v45
	v_fmac_f32_e32 v44, v64, v45
	s_waitcnt lgkmcnt(7)
	v_lshlrev_b32_e32 v45, 16, v102
	ds_read_u16 v102, v22 offset:35840
	v_fmac_f32_e32 v29, v80, v45
	v_fmac_f32_e32 v30, v79, v45
	v_fmac_f32_e32 v31, v78, v45
	v_fmac_f32_e32 v32, v77, v45
	v_fmac_f32_e32 v33, v76, v45
	v_fmac_f32_e32 v34, v75, v45
	v_fmac_f32_e32 v35, v74, v45
	v_fmac_f32_e32 v36, v73, v45
	v_fmac_f32_e32 v37, v72, v45
	v_fmac_f32_e32 v38, v71, v45
	v_fmac_f32_e32 v39, v70, v45
	v_fmac_f32_e32 v40, v69, v45
	v_fmac_f32_e32 v41, v68, v45
	v_fmac_f32_e32 v42, v67, v45
	v_fmac_f32_e32 v43, v66, v45
	v_fmac_f32_e32 v44, v65, v45
	s_waitcnt lgkmcnt(7)
	v_lshlrev_b32_e32 v45, 16, v103
	ds_read_u16 v103, v22 offset:36864
	v_fmac_f32_e32 v29, v81, v45
	v_fmac_f32_e32 v30, v80, v45
	v_fmac_f32_e32 v31, v79, v45
	v_fmac_f32_e32 v32, v78, v45
	v_fmac_f32_e32 v33, v77, v45
	v_fmac_f32_e32 v34, v76, v45
	v_fmac_f32_e32 v35, v75, v45
	v_fmac_f32_e32 v36, v74, v45
	v_fmac_f32_e32 v37, v73, v45
	v_fmac_f32_e32 v38, v72, v45
	v_fmac_f32_e32 v39, v71, v45
	v_fmac_f32_e32 v40, v70, v45
	v_fmac_f32_e32 v41, v69, v45
	v_fmac_f32_e32 v42, v68, v45
	v_fmac_f32_e32 v43, v67, v45
	v_fmac_f32_e32 v44, v66, v45
	s_waitcnt lgkmcnt(7)
	v_lshlrev_b32_e32 v45, 16, v104
	ds_read_u16 v104, v22 offset:37888
	v_fmac_f32_e32 v29, v82, v45
	v_fmac_f32_e32 v30, v81, v45
	v_fmac_f32_e32 v31, v80, v45
	v_fmac_f32_e32 v32, v79, v45
	v_fmac_f32_e32 v33, v78, v45
	v_fmac_f32_e32 v34, v77, v45
	v_fmac_f32_e32 v35, v76, v45
	v_fmac_f32_e32 v36, v75, v45
	v_fmac_f32_e32 v37, v74, v45
	v_fmac_f32_e32 v38, v73, v45
	v_fmac_f32_e32 v39, v72, v45
	v_fmac_f32_e32 v40, v71, v45
	v_fmac_f32_e32 v41, v70, v45
	v_fmac_f32_e32 v42, v69, v45
	v_fmac_f32_e32 v43, v68, v45
	v_fmac_f32_e32 v44, v67, v45
	s_waitcnt lgkmcnt(7)
	v_lshlrev_b32_e32 v45, 16, v105
	ds_read_u16 v105, v22 offset:38912
	v_fmac_f32_e32 v29, v83, v45
	v_fmac_f32_e32 v30, v82, v45
	v_fmac_f32_e32 v31, v81, v45
	v_fmac_f32_e32 v32, v80, v45
	v_fmac_f32_e32 v33, v79, v45
	v_fmac_f32_e32 v34, v78, v45
	v_fmac_f32_e32 v35, v77, v45
	v_fmac_f32_e32 v36, v76, v45
	v_fmac_f32_e32 v37, v75, v45
	v_fmac_f32_e32 v38, v74, v45
	v_fmac_f32_e32 v39, v73, v45
	v_fmac_f32_e32 v40, v72, v45
	v_fmac_f32_e32 v41, v71, v45
	v_fmac_f32_e32 v42, v70, v45
	v_fmac_f32_e32 v43, v69, v45
	v_fmac_f32_e32 v44, v68, v45
	s_waitcnt lgkmcnt(7)
	v_lshlrev_b32_e32 v45, 16, v106
	ds_read_u16 v106, v22 offset:39936
	v_fmac_f32_e32 v30, v83, v45
	v_fmac_f32_e32 v31, v82, v45
	v_fmac_f32_e32 v32, v81, v45
	v_fmac_f32_e32 v33, v80, v45
	v_fmac_f32_e32 v34, v79, v45
	v_fmac_f32_e32 v35, v78, v45
	v_fmac_f32_e32 v36, v77, v45
	v_fmac_f32_e32 v37, v76, v45
	v_fmac_f32_e32 v38, v75, v45
	v_fmac_f32_e32 v39, v74, v45
	v_fmac_f32_e32 v40, v73, v45
	v_fmac_f32_e32 v41, v72, v45
	v_fmac_f32_e32 v42, v71, v45
	v_fmac_f32_e32 v43, v70, v45
	v_fmac_f32_e32 v44, v69, v45
	s_waitcnt lgkmcnt(7)
	v_lshlrev_b32_e32 v45, 16, v107
	ds_read_u16 v107, v22 offset:40960
	v_fmac_f32_e32 v31, v83, v45
	v_fmac_f32_e32 v32, v82, v45
	v_fmac_f32_e32 v33, v81, v45
	v_fmac_f32_e32 v34, v80, v45
	v_fmac_f32_e32 v35, v79, v45
	v_fmac_f32_e32 v36, v78, v45
	v_fmac_f32_e32 v37, v77, v45
	v_fmac_f32_e32 v38, v76, v45
	v_fmac_f32_e32 v39, v75, v45
	v_fmac_f32_e32 v40, v74, v45
	v_fmac_f32_e32 v41, v73, v45
	v_fmac_f32_e32 v42, v72, v45
	v_fmac_f32_e32 v43, v71, v45
	v_fmac_f32_e32 v44, v70, v45
	s_waitcnt lgkmcnt(7)
	v_lshlrev_b32_e32 v45, 16, v100
	ds_read_u16 v100, v22 offset:41984
	v_fmac_f32_e32 v32, v83, v45
	v_fmac_f32_e32 v33, v82, v45
	v_fmac_f32_e32 v34, v81, v45
	v_fmac_f32_e32 v35, v80, v45
	v_fmac_f32_e32 v36, v79, v45
	v_fmac_f32_e32 v37, v78, v45
	v_fmac_f32_e32 v38, v77, v45
	v_fmac_f32_e32 v39, v76, v45
	v_fmac_f32_e32 v40, v75, v45
	v_fmac_f32_e32 v41, v74, v45
	v_fmac_f32_e32 v42, v73, v45
	v_fmac_f32_e32 v43, v72, v45
	v_fmac_f32_e32 v44, v71, v45
	s_waitcnt lgkmcnt(7)
	v_lshlrev_b32_e32 v45, 16, v101
	ds_read_u16 v101, v22 offset:43008
	v_fmac_f32_e32 v33, v83, v45
	v_fmac_f32_e32 v34, v82, v45
	v_fmac_f32_e32 v35, v81, v45
	v_fmac_f32_e32 v36, v80, v45
	v_fmac_f32_e32 v37, v79, v45
	v_fmac_f32_e32 v38, v78, v45
	v_fmac_f32_e32 v39, v77, v45
	v_fmac_f32_e32 v40, v76, v45
	v_fmac_f32_e32 v41, v75, v45
	v_fmac_f32_e32 v42, v74, v45
	v_fmac_f32_e32 v43, v73, v45
	v_fmac_f32_e32 v44, v72, v45
	s_waitcnt lgkmcnt(7)
	v_lshlrev_b32_e32 v45, 16, v102
	ds_read_u16 v102, v22 offset:44032
	v_fmac_f32_e32 v34, v83, v45
	v_fmac_f32_e32 v35, v82, v45
	v_fmac_f32_e32 v36, v81, v45
	v_fmac_f32_e32 v37, v80, v45
	v_fmac_f32_e32 v38, v79, v45
	v_fmac_f32_e32 v39, v78, v45
	v_fmac_f32_e32 v40, v77, v45
	v_fmac_f32_e32 v41, v76, v45
	v_fmac_f32_e32 v42, v75, v45
	v_fmac_f32_e32 v43, v74, v45
	v_fmac_f32_e32 v44, v73, v45
	s_waitcnt lgkmcnt(7)
	v_lshlrev_b32_e32 v45, 16, v103
	ds_read_u16 v103, v22 offset:45056
	v_fmac_f32_e32 v35, v83, v45
	v_fmac_f32_e32 v36, v82, v45
	v_fmac_f32_e32 v37, v81, v45
	v_fmac_f32_e32 v38, v80, v45
	v_fmac_f32_e32 v39, v79, v45
	v_fmac_f32_e32 v40, v78, v45
	v_fmac_f32_e32 v41, v77, v45
	v_fmac_f32_e32 v42, v76, v45
	v_fmac_f32_e32 v43, v75, v45
	v_fmac_f32_e32 v44, v74, v45
	s_waitcnt lgkmcnt(7)
	v_lshlrev_b32_e32 v45, 16, v104
	ds_read_u16 v104, v22 offset:46080
	v_fmac_f32_e32 v36, v83, v45
	v_fmac_f32_e32 v37, v82, v45
	v_fmac_f32_e32 v38, v81, v45
	v_fmac_f32_e32 v39, v80, v45
	v_fmac_f32_e32 v40, v79, v45
	v_fmac_f32_e32 v41, v78, v45
	v_fmac_f32_e32 v42, v77, v45
	v_fmac_f32_e32 v43, v76, v45
	v_fmac_f32_e32 v44, v75, v45
	s_waitcnt lgkmcnt(7)
	v_lshlrev_b32_e32 v45, 16, v105
	v_fmac_f32_e32 v37, v83, v45
	v_fmac_f32_e32 v38, v82, v45
	v_fmac_f32_e32 v39, v81, v45
	v_fmac_f32_e32 v40, v80, v45
	v_fmac_f32_e32 v41, v79, v45
	v_fmac_f32_e32 v42, v78, v45
	v_fmac_f32_e32 v43, v77, v45
	v_fmac_f32_e32 v44, v76, v45
	s_waitcnt lgkmcnt(6)
	v_lshlrev_b32_e32 v45, 16, v106
	v_fmac_f32_e32 v38, v83, v45
	v_fmac_f32_e32 v39, v82, v45
	v_fmac_f32_e32 v40, v81, v45
	v_fmac_f32_e32 v41, v80, v45
	v_fmac_f32_e32 v42, v79, v45
	v_fmac_f32_e32 v43, v78, v45
	v_fmac_f32_e32 v44, v77, v45
	s_waitcnt lgkmcnt(5)
	v_lshlrev_b32_e32 v45, 16, v107
	v_fmac_f32_e32 v39, v83, v45
	v_fmac_f32_e32 v40, v82, v45
	v_fmac_f32_e32 v41, v81, v45
	v_fmac_f32_e32 v42, v80, v45
	v_fmac_f32_e32 v43, v79, v45
	v_fmac_f32_e32 v44, v78, v45
	s_waitcnt lgkmcnt(4)
	v_lshlrev_b32_e32 v45, 16, v100
	v_fmac_f32_e32 v40, v83, v45
	v_fmac_f32_e32 v41, v82, v45
	v_fmac_f32_e32 v42, v81, v45
	v_fmac_f32_e32 v43, v80, v45
	v_fmac_f32_e32 v44, v79, v45
	s_waitcnt lgkmcnt(3)
	v_lshlrev_b32_e32 v45, 16, v101
	v_fmac_f32_e32 v41, v83, v45
	v_fmac_f32_e32 v42, v82, v45
	v_fmac_f32_e32 v43, v81, v45
	v_fmac_f32_e32 v44, v80, v45
	s_waitcnt lgkmcnt(2)
	v_lshlrev_b32_e32 v45, 16, v102
	v_fmac_f32_e32 v42, v83, v45
	v_fmac_f32_e32 v43, v82, v45
	v_fmac_f32_e32 v44, v81, v45
	s_waitcnt lgkmcnt(1)
	v_lshlrev_b32_e32 v45, 16, v103
	v_fmac_f32_e32 v43, v83, v45
	v_fmac_f32_e32 v44, v82, v45
	s_waitcnt lgkmcnt(0)
	v_lshlrev_b32_e32 v45, 16, v104
	v_fmac_f32_e32 v44, v83, v45
	ds_write2st64_b32 v23, v29, v30 offset1:8
	ds_write2st64_b32 v23, v31, v32 offset0:16 offset1:24
	ds_write2st64_b32 v23, v33, v34 offset0:32 offset1:40
	ds_write2st64_b32 v23, v35, v36 offset0:48 offset1:56
	ds_write2st64_b32 v23, v37, v38 offset0:64 offset1:72
	ds_write2st64_b32 v23, v39, v40 offset0:80 offset1:88
	ds_write2st64_b32 v23, v41, v42 offset0:96 offset1:104
	ds_write2st64_b32 v23, v43, v44 offset0:112 offset1:120
	v_add_u32_e32 v29, s36, v24
	v_cmp_gt_i32_e32 vcc, 64, v29
	s_waitcnt lgkmcnt(0)
	s_barrier
	s_and_saveexec_b64 s[34:35], vcc
	s_cbranch_execz .LBB0_2167
	ds_read_b128 v[30:33], v27
	ds_read_b128 v[34:37], v27 offset:16
	s_waitcnt lgkmcnt(1)
	v_mov_b32_e32 v38, v31
	v_mov_b32_e32 v39, v32
	v_mov_b32_e32 v40, v30
	v_mov_b32_e32 v41, v33
	v_pk_add_f32 v[38:39], v[38:39], v[40:41]
	s_waitcnt lgkmcnt(0)
	v_mov_b32_e32 v40, v36
	v_mov_b32_e32 v41, v34
	v_mov_b32_e32 v42, v37
	v_mov_b32_e32 v43, v35
	v_pk_add_f32 v[40:41], v[40:41], v[42:43]
	v_add_f32_e32 v29, v38, v39
	v_add_f32_e32 v29, v29, v41
	v_add_f32_e32 v29, v40, v29
	v_and_b32_e32 v39, 64, v214
	v_xor_b32_e32 v38, 16, v214
	v_add_f32_dpp v29, v29, v29 quad_perm:[1,0,3,2] row_mask:0xf bank_mask:0xf bound_ctrl:1
	v_add_u32_e32 v39, 64, v39
	v_cmp_lt_i32_e32 vcc, v38, v39
	v_add_f32_dpp v29, v29, v29 quad_perm:[2,3,0,1] row_mask:0xf bank_mask:0xf bound_ctrl:1
	s_nop 0
	v_cndmask_b32_e32 v38, v214, v38, vcc
	v_add_f32_dpp v29, v29, v29 row_half_mirror row_mask:0xf bank_mask:0xf bound_ctrl:1
	v_lshlrev_b32_e32 v46, 2, v38
	s_nop 0
	v_add_f32_dpp v29, v29, v29 row_mirror row_mask:0xf bank_mask:0xf bound_ctrl:1
	ds_bpermute_b32 v38, v46, v29
	s_waitcnt lgkmcnt(0)
	v_add_f32_e32 v29, v29, v38
	v_xor_b32_e32 v38, 32, v214
	v_cmp_lt_i32_e32 vcc, v38, v39
	s_nop 1
	v_cndmask_b32_e32 v38, v214, v38, vcc
	v_lshlrev_b32_e32 v47, 2, v38
	ds_bpermute_b32 v38, v47, v29
	s_waitcnt lgkmcnt(0)
	v_add_f32_e32 v29, v29, v38
	v_fmamk_f32 v31, v29, 0xbb000000, v31
	v_fmamk_f32 v30, v29, 0xbb000000, v30
	v_fmamk_f32 v33, v29, 0xbb000000, v33
	v_fmac_f32_e32 v32, 0xbb000000, v29
	v_pk_mul_f32 v[38:39], v[32:33], v[32:33]
	v_pk_mul_f32 v[40:41], v[30:31], v[30:31]
	v_fmamk_f32 v35, v29, 0xbb000000, v35
	v_fmamk_f32 v34, v29, 0xbb000000, v34
	v_fmamk_f32 v37, v29, 0xbb000000, v37
	v_fmac_f32_e32 v36, 0xbb000000, v29
	v_pk_mov_b32 v[42:43], v[40:41], v[38:39] op_sel:[1,0]
	v_mov_b32_e32 v41, v39
	v_pk_add_f32 v[38:39], v[42:43], v[40:41]
	v_pk_mul_f32 v[40:41], v[36:37], v[36:37]
	v_pk_mul_f32 v[42:43], v[34:35], v[34:35]
	v_mov_b32_e32 v44, v40
	v_mov_b32_e32 v45, v42
	v_mov_b32_e32 v42, v41
	v_pk_add_f32 v[40:41], v[44:45], v[42:43]
	v_add_f32_e32 v29, v38, v39
	v_add_f32_e32 v29, v41, v29
	v_add_f32_e32 v29, v40, v29
	s_nop 1
	v_add_f32_dpp v29, v29, v29 quad_perm:[1,0,3,2] row_mask:0xf bank_mask:0xf bound_ctrl:1
	s_nop 1
	v_add_f32_dpp v29, v29, v29 quad_perm:[2,3,0,1] row_mask:0xf bank_mask:0xf bound_ctrl:1
	s_nop 1
	v_add_f32_dpp v29, v29, v29 row_half_mirror row_mask:0xf bank_mask:0xf bound_ctrl:1
	s_nop 1
	v_add_f32_dpp v29, v29, v29 row_mirror row_mask:0xf bank_mask:0xf bound_ctrl:1
	ds_bpermute_b32 v38, v46, v29
	s_waitcnt lgkmcnt(0)
	v_add_f32_e32 v29, v29, v38
	ds_bpermute_b32 v38, v47, v29
	s_waitcnt lgkmcnt(0)
	v_add_f32_e32 v29, v29, v38
	v_fmamk_f32 v29, v29, 0x3b000000, v1
	v_mul_f32_e32 v38, 0x4b800000, v29
	v_cmp_gt_f32_e32 vcc, s77, v29
	s_nop 1
	v_cndmask_b32_e32 v29, v29, v38, vcc
	v_rsq_f32_e32 v29, v29
	s_nop 0
	v_mul_f32_e32 v38, 0x45800000, v29
	v_cndmask_b32_e32 v38, v29, v38, vcc
	v_pk_mul_f32 v[30:31], v[30:31], v[38:39] op_sel_hi:[1,0]
	v_pk_mul_f32 v[34:35], v[34:35], v[38:39] op_sel_hi:[1,0]
	v_pk_fma_f32 v[30:31], v[6:7], v[30:31], v[14:15]
	v_pk_fma_f32 v[34:35], v[2:3], v[34:35], v[10:11]
	v_mul_f32_e32 v29, 0xbfb8aa3b, v30
	v_pk_mul_f32 v[32:33], v[32:33], v[38:39] op_sel_hi:[1,0]
	v_pk_mul_f32 v[36:37], v[36:37], v[38:39] op_sel_hi:[1,0]
	v_exp_f32_e32 v29, v29
	v_mul_f32_e32 v38, 0xbfb8aa3b, v34
	v_exp_f32_e32 v39, v38
	v_mul_f32_e32 v40, 0xbfb8aa3b, v35
	v_add_f32_e32 v29, 1.0, v29
	v_rcp_f32_e32 v38, v29
	v_add_f32_e32 v29, 1.0, v39
	v_mul_f32_e32 v39, 0xbfb8aa3b, v31
	v_exp_f32_e32 v39, v39
	v_exp_f32_e32 v41, v40
	v_pk_fma_f32 v[32:33], v[8:9], v[32:33], v[16:17]
	v_rcp_f32_e32 v40, v29
	v_add_f32_e32 v29, 1.0, v39
	v_pk_fma_f32 v[36:37], v[4:5], v[36:37], v[12:13]
	v_rcp_f32_e32 v39, v29
	v_add_f32_e32 v29, 1.0, v41
	v_mul_f32_e32 v41, 0xbfb8aa3b, v32
	v_exp_f32_e32 v42, v41
	v_mul_f32_e32 v41, 0xbfb8aa3b, v36
	v_exp_f32_e32 v43, v41
	v_rcp_f32_e32 v41, v29
	v_add_f32_e32 v29, 1.0, v42
	v_rcp_f32_e32 v42, v29
	v_add_f32_e32 v29, 1.0, v43
	v_mul_f32_e32 v43, 0xbfb8aa3b, v33
	v_exp_f32_e32 v43, v43
	v_mul_f32_e32 v44, 0xbfb8aa3b, v37
	v_exp_f32_e32 v45, v44
	v_rcp_f32_e32 v44, v29
	v_add_f32_e32 v29, 1.0, v43
	v_rcp_f32_e32 v43, v29
	v_add_f32_e32 v29, 1.0, v45
	v_rcp_f32_e32 v45, v29
	v_pk_mul_f32 v[30:31], v[30:31], v[38:39]
	v_pk_mul_f32 v[34:35], v[34:35], v[40:41]
	v_pk_mul_f32 v[32:33], v[32:33], v[42:43]
	v_cvt_pk_bf16_f32 v30, v30, v31
	v_cvt_pk_bf16_f32 v31, v32, v33
	v_cvt_pk_bf16_f32 v32, v34, v35
	v_add_u32_e32 v34, s36, v26
	v_ashrrev_i32_e32 v35, 31, v34
	v_pk_mul_f32 v[36:37], v[36:37], v[44:45]
	v_lshlrev_b64 v[34:35], 11, v[34:35]
	v_cvt_pk_bf16_f32 v33, v36, v37
	v_lshl_add_u64 v[34:35], v[18:19], 0, v[34:35]
	global_store_dwordx4 v[34:35], v[30:33], off offset:1024
